# baseline (speedup 1.0000x reference)
.LBB1_235:
	v_add_u32_e32 v0, s66, v0
	v_subrev_u32_e32 v0, 0x100, v0
	s_movk_i32 s0, 0xf0
	v_cmp_gt_u32_e32 vcc, s0, v0
	s_and_saveexec_b64 s[0:1], vcc
	s_cbranch_execz .Lepi_idle
	s_load_dwordx4 s[68:71], s[14:15], 0x0
	s_load_dwordx2 s[72:73], s[14:15], 0x10
	s_movk_i32 s0, 0x77
	v_mov_b32_e32 v1, 0xffffff88
	v_cmp_lt_u32_e32 vcc, s0, v0
	v_mov_b32_e32 v2, 0x44704000
	s_mov_b32 s0, 0xf800000
	v_cndmask_b32_e32 v1, 0, v1, vcc
	v_add_u32_e32 v0, v1, v0
	v_cvt_f32_u32_e32 v1, v0
	s_mov_b32 s5, 0x17800
	s_mov_b32 s4, 0x3eb17218
	v_fmac_f32_e32 v2, 0xc1000000, v1
	v_sqrt_f32_e32 v1, v2
	s_nop 0
	v_sub_f32_e32 v1, 0x41f80000, v1
	v_mul_f32_e32 v1, 0.5, v1
	v_cvt_i32_f32_e32 v1, v1
	s_and_b64 s[0:1], exec, s[16:17]
	s_cselect_b32 s2, s40, s38
	s_cselect_b32 s3, s39, s33
	v_sub_u32_e32 v2, 31, v1
	v_mul_u32_u24_e32 v2, v2, v1
	v_lshrrev_b32_e32 v2, 1, v2
	v_cmp_gt_i32_e64 s[0:1], v2, v0
	s_nop 1
	v_subbrev_co_u32_e64 v1, s[0:1], 0, v1, s[0:1]
	v_add_u32_e32 v2, 1, v1
	v_sub_u32_e32 v3, 30, v1
	v_mul_u32_u24_e32 v3, v2, v3
	v_lshrrev_b32_e32 v3, 1, v3
	v_cmp_gt_i32_e64 s[0:1], v3, v0
	s_nop 1
	v_cndmask_b32_e64 v12, v2, v1, s[0:1]
	v_sub_u32_e32 v1, 31, v12
	v_mul_u32_u24_e32 v1, v1, v12
	v_lshrrev_b32_e32 v1, 1, v1
	v_sub_u32_e32 v0, v0, v1
	v_cndmask_b32_e64 v1, 0, 16, vcc
	v_lshl_or_b32 v1, s2, 5, v1
	v_add_u32_e32 v1, v1, v12
	v_sub_u32_e32 v2, 0xff, v1
	v_mul_u32_u24_e32 v1, v2, v1
	v_lshrrev_b32_e32 v1, 1, v1
	v_add3_u32 v13, v12, v0, 1
	v_add_u32_e32 v0, v1, v0
	s_mul_i32 s3, s3, 0x1fc0
	v_add_u32_e32 v0, s3, v0
	v_mul_u32_u24_e32 v4, 24, v0
	v_mov_b32_e32 v0, 0x17800
	v_lshl_add_u32 v14, v12, 2, v0
	v_mov_b32_e32 v0, 0x60
	v_cndmask_b32_e32 v15, 0, v0, vcc
	v_lshlrev_b32_e32 v16, 2, v13
	v_add_lshl_u32 v0, v15, v12, 6
	v_add3_u32 v16, v0, v16, s5
	v_add_u32_e32 v1, v15, v13
	v_lshl_add_u32 v17, v1, 6, v14
	ds_read_b32 v0, v16
	ds_read_b32 v2, v17
	ds_read_b32 v1, v16 offset:1024
	ds_read_b32 v3, v17 offset:1024
	ds_read_b32 v6, v16 offset:2048
	ds_read_b32 v8, v17 offset:2048
	ds_read_b32 v7, v16 offset:3072
	ds_read_b32 v9, v17 offset:3072
	ds_read_b32 v12, v16 offset:4096
	ds_read_b32 v14, v17 offset:4096
	ds_read_b32 v13, v16 offset:5120
	ds_read_b32 v15, v17 offset:5120
	s_waitcnt lgkmcnt(0)
	v_pk_add_f32 v[0:1], v[0:1], v[2:3]
	v_mov_b32_e32 v2, s70
	v_mov_b32_e32 v3, s71
	v_mov_b64_e32 v[10:11], s[68:69]
	v_pk_add_f32 v[6:7], v[6:7], v[8:9]
	v_pk_fma_f32 v[0:1], v[0:1], s[4:5], v[10:11] op_sel_hi:[1,0,1]
	v_pk_fma_f32 v[2:3], v[6:7], s[4:5], v[2:3] op_sel_hi:[1,0,1]
	global_store_dwordx4 v4, v[0:3], s[10:11]
	s_nop 1
	v_pk_add_f32 v[0:1], v[12:13], v[14:15]
	v_mov_b64_e32 v[2:3], s[72:73]
	v_pk_fma_f32 v[0:1], v[0:1], s[4:5], v[2:3] op_sel_hi:[1,0,1]
	global_store_dwordx2 v4, v[0:1], s[10:11] offset:16
	s_endpgm
